# speedup vs baseline: 1.0027x; 1.0027x over previous
.LBB0_17:
	v_lshrrev_b32_e32 v3, 3, v7
	v_lshrrev_b32_e32 v20, 3, v6
	v_ashrrev_i32_e32 v21, 7, v7
	v_ashrrev_i32_e32 v22, 7, v6
	v_lshrrev_b32_e32 v23, 5, v7
	v_lshrrev_b32_e32 v24, 5, v6
	v_and_b32_e32 v21, 0xffffffe0, v21
	v_and_b32_e32 v22, 0xffffffe0, v22
	v_and_b32_e32 v3, 31, v3
	v_and_b32_e32 v20, 31, v20
	v_and_b32_e32 v25, 0x70, v23
	v_and_b32_e32 v26, 0x70, v24
	v_and_b32_e32 v23, 8, v23
	v_and_b32_e32 v24, 8, v24
	v_or_b32_e32 v3, v21, v3
	v_or_b32_e32 v20, v22, v20
	v_or_b32_e32 v21, v23, v1
	v_or_b32_e32 v22, v24, v4
	v_or_b32_e32 v21, v21, v25
	v_or_b32_e32 v22, v22, v26
	v_lshlrev_b32_e32 v23, 6, v3
	v_lshlrev_b32_e32 v24, 6, v20
	v_lshlrev_b32_e32 v27, 7, v20
	v_lshlrev_b32_e32 v3, 7, v3
	v_add3_u32 v28, v21, v23, s25
	v_or_b32_e32 v23, v23, v21
	v_cmp_gt_u32_e32 vcc, 64, v25
	v_add3_u32 v25, v22, v24, s25
	v_or_b32_e32 v24, v24, v22
	v_or_b32_e32 v22, v27, v22
	v_cmp_gt_u32_e64 s[2:3], 64, v26
	v_or_b32_e32 v20, v3, v21
	v_cndmask_b32_e32 v26, v28, v23, vcc
	v_cndmask_b32_e64 v24, v25, v24, s[2:3]
	v_ashrrev_i32_e32 v23, 31, v22
	v_cndmask_b32_e32 v29, v11, v12, vcc
	v_cndmask_b32_e32 v28, v13, v14, vcc
	v_cndmask_b32_e64 v31, v15, v16, s[2:3]
	v_cndmask_b32_e64 v30, v17, v18, s[2:3]
	v_ashrrev_i32_e32 v21, 31, v20
	v_ashrrev_i32_e32 v27, 31, v26
	v_ashrrev_i32_e32 v25, 31, v24
	v_lshl_add_u64 v[22:23], v[22:23], 2, s[16:17]
	v_lshl_add_u64 v[20:21], v[20:21], 2, s[16:17]
	v_lshl_add_u64 v[24:25], v[24:25], 2, v[30:31]
	v_lshl_add_u64 v[26:27], v[26:27], 2, v[28:29]
	global_load_dword v3, v[22:23], off nt
	global_load_dword v28, v[20:21], off nt
	global_load_dword v29, v[24:25], off nt
	global_load_dword v30, v[26:27], off nt
	v_ashrrev_i32_e32 v23, 31, v6
	v_mov_b32_e32 v22, v6
	v_add_u32_e32 v19, -2, v19
	v_ashrrev_i32_e32 v21, 31, v7
	v_mov_b32_e32 v20, v7
	v_lshlrev_b64 v[22:23], 1, v[22:23]
	v_cmp_eq_u32_e32 vcc, 0, v19
	v_add_u32_e32 v7, s24, v7
	v_add_u32_e32 v6, s13, v6
	v_lshlrev_b64 v[20:21], 1, v[20:21]
	v_lshl_add_u64 v[24:25], s[4:5], 0, v[22:23]
	v_lshl_add_u64 v[22:23], s[6:7], 0, v[22:23]
	s_or_b64 s[20:21], vcc, s[20:21]
	v_lshl_add_u64 v[26:27], s[4:5], 0, v[20:21]
	v_lshl_add_u64 v[20:21], s[6:7], 0, v[20:21]
	s_waitcnt vmcnt(2)
	v_cvt_pk_f16_f32 v3, v3, v28
	s_waitcnt vmcnt(0)
	v_cvt_pk_f16_f32 v28, v29, v30
	global_store_short v[22:23], v3, off sc1
	global_store_short_d16_hi v[20:21], v3, off sc1
	global_store_short v[24:25], v28, off sc1
	global_store_short_d16_hi v[26:27], v28, off sc1
	s_andn2_b64 exec, exec, s[20:21]
	s_cbranch_execnz .LBB0_17
	s_or_b64 exec, exec, s[20:21]
	v_mad_u64_u32 v[6:7], s[2:3], v9, s12, v[2:3]
	v_cmp_ne_u32_e32 vcc, v8, v9
	s_orn2_b64 s[2:3], vcc, exec

.LBB0_21:
	v_lshrrev_b32_e32 v12, 3, v6
	v_ashrrev_i32_e32 v13, 7, v6
	v_lshrrev_b32_e32 v14, 5, v6
	v_bfi_b32 v12, s13, v13, v12
	v_and_b32_e32 v13, 0x70, v14
	v_and_b32_e32 v14, 8, v14
	v_or3_b32 v14, v14, v4, v13
	v_lshlrev_b32_e32 v15, 6, v12
	v_add3_u32 v16, v14, v15, s20
	v_or_b32_e32 v15, v15, v14
	v_lshl_or_b32 v12, v12, 7, v14
	v_cmp_gt_u32_e32 vcc, 64, v13
	v_ashrrev_i32_e32 v13, 31, v12
	v_lshl_add_u64 v[12:13], v[12:13], 2, s[16:17]
	v_cndmask_b32_e32 v14, v16, v15, vcc
	v_cndmask_b32_e32 v17, v1, v3, vcc
	v_cndmask_b32_e32 v16, v7, v11, vcc
	v_ashrrev_i32_e32 v15, 31, v14
	v_lshl_add_u64 v[14:15], v[14:15], 2, v[16:17]
	global_load_dword v16, v[12:13], off nt
	global_load_dword v17, v[14:15], off nt
	v_add_u32_e32 v6, s12, v6
	v_cmp_lt_i32_e32 vcc, s8, v6
	v_lshl_add_u64 v[12:13], s[4:5], 0, v[8:9]
	v_lshl_add_u64 v[14:15], s[6:7], 0, v[8:9]
	v_lshl_add_u64 v[8:9], v[8:9], 0, s[2:3]
	s_or_b64 s[18:19], vcc, s[18:19]
	s_waitcnt vmcnt(1)
	v_cvt_f16_f32_e32 v16, v16
	s_waitcnt vmcnt(0)
	v_cvt_f16_f32_e32 v17, v17
	global_store_short v[14:15], v16, off sc1
	global_store_short v[12:13], v17, off sc1
	s_andn2_b64 exec, exec, s[18:19]
	s_cbranch_execnz .LBB0_21
.LBB0_22:
	s_or_b64 exec, exec, s[14:15]
	s_movk_i32 s2, 0x80
	v_cmp_gt_i32_e32 vcc, s2, v2
	s_and_saveexec_b64 s[2:3], vcc
	s_cbranch_execz .LBB0_24
	s_waitcnt lgkmcnt(0)
	s_load_dwordx4 s[4:7], s[0:1], 0x38
	v_mov_b32_e32 v3, 0
	v_lshlrev_b64 v[6:7], 2, v[2:3]
	s_waitcnt lgkmcnt(0)
	v_lshl_add_u64 v[12:13], s[4:5], 0, v[6:7]
	v_lshl_add_u64 v[8:9], s[6:7], 0, v[6:7]
	global_load_dword v1, v[12:13], off nt
	global_load_dword v3, v[8:9], off nt
	s_load_dwordx2 s[4:5], s[0:1], 0x58
	s_waitcnt lgkmcnt(0)
	v_lshl_add_u64 v[6:7], s[4:5], 0, v[6:7]
	s_waitcnt vmcnt(0)
	v_add_f32_e32 v1, v1, v3
	global_store_dword v[6:7], v1, off sc1

.LBB3_26:
	s_or_b64 exec, exec, s[0:1]
	v_and_b32_e32 v62, 63, v0
	v_bfe_u32 v63, v0, 5, 1
	v_lshrrev_b32_e32 v64, 6, v0
	v_and_b32_e32 v65, 31, v0
	s_setprio 0
	s_waitcnt vmcnt(1)
	v_lshlrev_b32_e32 v10, 4, v62
	v_lshl_or_b32 v10, v64, 13, v10
	v_mov_b32_e32 v11, 0
	v_lshl_add_u64 v[12:13], s[12:13], 0, v[10:11]
	s_movk_i32 s0, 0x1000
	s_waitcnt lgkmcnt(0)
	global_load_dwordx4 v[6:9], v[38:39], off
	global_load_dwordx4 v[2:5], v[40:41], off
	global_load_dwordx4 v[16:19], v10, s[12:13]
	global_load_dwordx4 v[56:59], v10, s[12:13] offset:1024
	global_load_dwordx4 v[52:55], v10, s[12:13] offset:2048
	global_load_dwordx4 v[48:51], v10, s[12:13] offset:3072
	v_add_co_u32_e32 v10, vcc, s0, v12
	v_lshrrev_b32_e32 v23, 4, v0
	s_nop 0
	v_addc_co_u32_e32 v11, vcc, 0, v13, vcc
	global_load_dwordx4 v[44:47], v[10:11], off
	global_load_dwordx4 v[40:43], v[10:11], off offset:1024
	global_load_dwordx4 v[36:39], v[10:11], off offset:2048
	global_load_dwordx4 v[32:35], v[10:11], off offset:3072
	v_lshlrev_b32_e32 v10, 1, v0
	v_and_b32_e32 v11, 28, v10
	v_lshlrev_b32_e32 v10, 8, v0
	v_and_b32_e32 v21, 0x100, v10
	v_mul_u32_u24_e32 v10, 0x220, v23
	v_or_b32_e32 v10, v11, v10
	v_lshlrev_b32_e32 v0, 2, v23
	v_add_u32_e32 v26, v10, v21
	s_barrier
	ds_read_b32 v0, v0 offset:38912
	ds_read2_b32 v[12:13], v26 offset1:8
	ds_read2_b32 v[14:15], v26 offset0:16 offset1:24
	v_lshrrev_b32_e32 v66, 4, v84
	v_lshrrev_b32_e32 v67, 4, v83
	v_lshrrev_b32_e32 v68, 4, v82
	v_lshlrev_b32_e32 v10, 2, v66
	v_lshlrev_b32_e32 v22, 2, v67
	v_lshlrev_b32_e32 v24, 2, v68
	ds_read_b32 v20, v10 offset:38912
	ds_read_b32 v22, v22 offset:38912
	ds_read_b32 v10, v24 offset:38912
	ds_read2_b32 v[24:25], v26 offset0:32 offset1:40
	s_waitcnt lgkmcnt(5)
	v_fma_mixlo_f16 v69, v0, v12, 0
	v_mov_b32_e32 v12, v13
	s_waitcnt lgkmcnt(4)
	v_mov_b32_e32 v13, v14
	v_mul_f32_e32 v12, v0, v12
	v_mul_f32_e32 v13, v0, v13
	v_cvt_pk_f16_f32 v70, v12, v13
	v_mov_b32_e32 v12, v15
	s_waitcnt lgkmcnt(0)
	v_mov_b32_e32 v13, v24
	v_mul_f32_e32 v12, v0, v12
	v_mul_f32_e32 v13, v0, v13
	v_cvt_pk_f16_f32 v71, v12, v13
	v_mul_u32_u24_e32 v13, 0x220, v66
	ds_read2_b32 v[26:27], v26 offset0:48 offset1:56
	v_or_b32_e32 v13, v11, v13
	v_add_u32_e32 v28, v13, v21
	ds_read2_b32 v[14:15], v28 offset1:8
	v_mov_b32_e32 v12, v25
	s_waitcnt lgkmcnt(1)
	v_mov_b32_e32 v13, v26
	ds_read2_b32 v[24:25], v28 offset0:16 offset1:24
	v_mul_f32_e32 v12, v0, v12
	v_mul_f32_e32 v13, v0, v13
	v_cvt_pk_f16_f32 v26, v12, v13
	s_waitcnt lgkmcnt(1)
	v_fma_mixlo_f16 v72, v20, v14, 0
	v_mov_b32_e32 v12, v15
	ds_read2_b32 v[14:15], v28 offset0:32 offset1:40
	s_waitcnt lgkmcnt(1)
	v_mov_b32_e32 v13, v24
	v_mul_f32_e32 v12, v20, v12
	v_mul_f32_e32 v13, v20, v13
	v_cvt_pk_f16_f32 v73, v12, v13
	v_mov_b32_e32 v12, v25
	s_waitcnt lgkmcnt(0)
	v_mov_b32_e32 v13, v14
	v_mul_f32_e32 v12, v20, v12
	v_mul_f32_e32 v13, v20, v13
	v_cvt_pk_f16_f32 v74, v12, v13
	v_mul_u32_u24_e32 v13, 0x220, v67
	ds_read2_b32 v[24:25], v28 offset0:48 offset1:56
	v_or_b32_e32 v13, v11, v13
	v_add_u32_e32 v30, v13, v21
	v_mov_b32_e32 v12, v15
	ds_read2_b32 v[14:15], v30 offset1:8
	s_waitcnt lgkmcnt(1)
	v_mov_b32_e32 v13, v24
	ds_read2_b32 v[28:29], v30 offset0:16 offset1:24
	v_mul_f32_e32 v12, v20, v12
	v_mul_f32_e32 v13, v20, v13
	v_cvt_pk_f16_f32 v24, v12, v13
	s_waitcnt lgkmcnt(1)
	v_fma_mixlo_f16 v75, v22, v14, 0
	v_mov_b32_e32 v12, v15
	ds_read2_b32 v[14:15], v30 offset0:32 offset1:40
	s_waitcnt lgkmcnt(1)
	v_mov_b32_e32 v13, v28
	v_mul_f32_e32 v12, v22, v12
	v_mul_f32_e32 v13, v22, v13
	v_cvt_pk_f16_f32 v76, v12, v13
	v_mov_b32_e32 v12, v29
	s_waitcnt lgkmcnt(0)
	v_mov_b32_e32 v13, v14
	v_mul_f32_e32 v12, v22, v12
	v_mul_f32_e32 v13, v22, v13
	v_cvt_pk_f16_f32 v77, v12, v13
	v_mul_u32_u24_e32 v13, 0x220, v68
	ds_read2_b32 v[28:29], v30 offset0:48 offset1:56
	v_or_b32_e32 v11, v11, v13
	v_add_u32_e32 v11, v11, v21
	v_mov_b32_e32 v12, v15
	ds_read2_b32 v[14:15], v11 offset1:8
	ds_read2_b32 v[30:31], v11 offset0:16 offset1:24
	s_waitcnt lgkmcnt(2)
	v_mov_b32_e32 v13, v28
	v_mul_f32_e32 v12, v22, v12
	v_mul_f32_e32 v13, v22, v13
	v_cvt_pk_f16_f32 v21, v12, v13
	s_waitcnt lgkmcnt(1)
	v_fma_mixlo_f16 v28, v10, v14, 0
	v_mov_b32_e32 v12, v15
	s_waitcnt lgkmcnt(0)
	v_mov_b32_e32 v13, v30
	ds_read2_b32 v[14:15], v11 offset0:32 offset1:40
	v_mul_f32_e32 v12, v10, v12
	v_mul_f32_e32 v13, v10, v13
	v_cvt_pk_f16_f32 v78, v12, v13
	v_mov_b32_e32 v12, v31
	ds_read2_b32 v[30:31], v11 offset0:48 offset1:56
	s_waitcnt lgkmcnt(1)
	v_mov_b32_e32 v13, v14
	v_mul_f32_e32 v12, v10, v12
	v_mul_f32_e32 v13, v10, v13
	v_cvt_pk_f16_f32 v11, v12, v13
	v_mov_b32_e32 v12, v15
	s_waitcnt lgkmcnt(0)
	v_mov_b32_e32 v13, v30
	v_mul_f32_e32 v12, v10, v12
	v_mul_f32_e32 v13, v10, v13
	v_and_b32_e32 v79, 0xf0, v81
	v_lshrrev_b32_e32 v15, 16, v26
	s_movk_i32 s0, 0x110
	v_cvt_pk_f16_f32 v30, v12, v13
	v_pack_b32_f16 v12, v69, v70
	v_alignbit_b32 v13, v71, v70, 16
	v_alignbit_b32 v14, v26, v71, 16
	v_fma_mixhi_f16 v15, v0, v27, 0
	v_mad_u32_u24 v0, v23, s0, v79
	s_barrier
	ds_write_b128 v0, v[12:15]
	v_lshrrev_b32_e32 v15, 16, v24
	v_pack_b32_f16 v12, v72, v73
	v_alignbit_b32 v13, v74, v73, 16
	v_alignbit_b32 v14, v24, v74, 16
	v_fma_mixhi_f16 v15, v20, v25, 0
	v_mad_u32_u24 v0, v66, s0, v79
	ds_write_b128 v0, v[12:15]
	v_lshrrev_b32_e32 v15, 16, v21
	v_pack_b32_f16 v12, v75, v76
	v_alignbit_b32 v13, v77, v76, 16
	v_alignbit_b32 v14, v21, v77, 16
	v_fma_mixhi_f16 v15, v22, v29, 0
	v_mad_u32_u24 v0, v67, s0, v79
	ds_write_b128 v0, v[12:15]
	v_lshlrev_b32_e32 v0, 2, v80
	ds_read_b32 v0, v0 offset:38912
	v_lshrrev_b32_e32 v15, 16, v30
	v_fma_mixhi_f16 v15, v10, v31, 0
	v_lshlrev_b32_e32 v10, 2, v1
	ds_read_b32 v24, v10 offset:38912
	s_waitcnt lgkmcnt(1)
	v_div_scale_f32 v10, s[4:5], v0, v0, s18
	v_alignbit_b32 v13, v11, v78, 16
	v_alignbit_b32 v14, v30, v11, 16
	v_rcp_f32_e32 v11, v10
	v_pack_b32_f16 v12, v28, v78
	v_mad_u32_u24 v20, v68, s0, v79
	ds_write_b128 v20, v[12:15]
	v_fma_f32 v12, -v10, v11, 1.0
	v_fmac_f32_e32 v11, v12, v11
	v_div_scale_f32 v12, vcc, s18, v0, s18
	v_mul_f32_e32 v13, v12, v11
	v_fma_f32 v14, -v10, v13, v12
	v_fmac_f32_e32 v13, v14, v11
	v_fma_f32 v10, -v10, v13, v12
	v_div_fmas_f32 v10, v10, v11, v13
	v_div_fixup_f32 v0, v10, v0, s18
	s_waitcnt vmcnt(9)
	v_cvt_f32_ubyte1_e32 v13, v8
	v_cvt_f32_ubyte0_e32 v12, v8
	v_mul_f32_e32 v12, v0, v12
	v_mul_f32_e32 v13, v0, v13
	v_cvt_f32_ubyte1_e32 v11, v6
	v_cvt_f32_ubyte0_e32 v10, v6
	v_cvt_pk_f16_f32 v20, v12, v13
	v_cvt_f32_ubyte3_e32 v13, v6
	v_cvt_f32_ubyte2_e32 v12, v6
	v_mul_f32_e32 v10, v0, v10
	v_mul_f32_e32 v11, v0, v11
	v_mul_f32_e32 v12, v0, v12
	v_mul_f32_e32 v13, v0, v13
	v_cvt_pk_f16_f32 v10, v10, v11
	v_cvt_pk_f16_f32 v11, v12, v13
	v_cvt_f32_ubyte3_e32 v13, v8
	v_cvt_f32_ubyte2_e32 v12, v8
	v_cvt_f32_ubyte1_e32 v15, v9
	v_cvt_f32_ubyte0_e32 v14, v9
	v_mul_f32_e32 v12, v0, v12
	v_mul_f32_e32 v13, v0, v13
	v_mul_f32_e32 v14, v0, v14
	v_mul_f32_e32 v15, v0, v15
	v_cvt_pk_f16_f32 v21, v12, v13
	v_cvt_f32_ubyte1_e32 v13, v7
	v_cvt_f32_ubyte0_e32 v12, v7
	v_cvt_pk_f16_f32 v22, v14, v15
	v_cvt_f32_ubyte3_e32 v15, v7
	v_cvt_f32_ubyte2_e32 v14, v7
	v_mul_f32_e32 v12, v0, v12
	v_mul_f32_e32 v13, v0, v13
	v_mul_f32_e32 v6, v0, v14
	v_mul_f32_e32 v7, v0, v15
	v_cvt_pk_f16_f32 v12, v12, v13
	v_cvt_pk_f16_f32 v13, v6, v7
	v_cvt_f32_ubyte3_e32 v7, v9
	v_cvt_f32_ubyte2_e32 v6, v9
	v_mul_f32_e32 v6, v0, v6
	v_mul_f32_e32 v7, v0, v7
	s_waitcnt lgkmcnt(1)
	v_div_scale_f32 v0, s[4:5], v24, v24, s18
	v_cvt_pk_f16_f32 v23, v6, v7
	v_rcp_f32_e32 v6, v0
	v_lshlrev_b32_e32 v25, 1, v60
	v_mad_u32_u24 v7, v80, s0, v25
	ds_write_b128 v7, v[10:13] offset:17408
	ds_write_b128 v7, v[20:23] offset:17424
	v_fma_f32 v7, -v0, v6, 1.0
	v_fmac_f32_e32 v6, v7, v6
	v_div_scale_f32 v7, vcc, s18, v24, s18
	v_mul_f32_e32 v8, v7, v6
	v_fma_f32 v9, -v0, v8, v7
	v_fmac_f32_e32 v8, v9, v6
	v_fma_f32 v0, -v0, v8, v7
	v_div_fmas_f32 v0, v0, v6, v8
	v_div_fixup_f32 v0, v0, v24, s18
	s_waitcnt vmcnt(8)
	v_cvt_f32_ubyte1_e32 v9, v4
	v_cvt_f32_ubyte0_e32 v8, v4
	v_mul_f32_e32 v8, v0, v8
	v_mul_f32_e32 v9, v0, v9
	v_cvt_f32_ubyte1_e32 v7, v2
	v_cvt_f32_ubyte0_e32 v6, v2
	v_cvt_pk_f16_f32 v10, v8, v9
	v_cvt_f32_ubyte3_e32 v9, v2
	v_cvt_f32_ubyte2_e32 v8, v2
	v_mul_f32_e32 v6, v0, v6
	v_mul_f32_e32 v7, v0, v7
	v_mul_f32_e32 v8, v0, v8
	v_mul_f32_e32 v9, v0, v9
	v_cvt_pk_f16_f32 v6, v6, v7
	v_cvt_pk_f16_f32 v7, v8, v9
	v_cvt_f32_ubyte3_e32 v9, v4
	v_cvt_f32_ubyte2_e32 v8, v4
	v_mul_f32_e32 v8, v0, v8
	v_mul_f32_e32 v9, v0, v9
	v_cvt_pk_f16_f32 v11, v8, v9
	v_cvt_f32_ubyte1_e32 v9, v3
	v_cvt_f32_ubyte0_e32 v8, v3
	v_cvt_f32_ubyte3_e32 v15, v3
	v_cvt_f32_ubyte2_e32 v14, v3
	v_mul_f32_e32 v8, v0, v8
	v_mul_f32_e32 v9, v0, v9
	v_mul_f32_e32 v2, v0, v14
	v_mul_f32_e32 v3, v0, v15
	v_cvt_pk_f16_f32 v8, v8, v9
	v_cvt_f32_ubyte1_e32 v13, v5
	v_cvt_f32_ubyte0_e32 v12, v5
	v_cvt_pk_f16_f32 v9, v2, v3
	v_cvt_f32_ubyte3_e32 v3, v5
	v_cvt_f32_ubyte2_e32 v2, v5
	v_mul_f32_e32 v12, v0, v12
	v_mul_f32_e32 v13, v0, v13
	v_mul_f32_e32 v2, v0, v2
	v_mul_f32_e32 v3, v0, v3
	v_mad_u32_u24 v0, v1, s0, v25
	v_cvt_pk_f16_f32 v12, v12, v13
	v_cvt_pk_f16_f32 v13, v2, v3
	ds_write_b128 v0, v[6:9] offset:17408
	ds_write_b128 v0, v[10:13] offset:17424
	v_lshlrev_b32_e32 v0, 4, v63
	v_mad_u32_u24 v60, v65, s0, v0
	s_waitcnt lgkmcnt(0)
	s_barrier
	ds_read_b128 v[0:3], v60
	ds_read_b128 v[66:69], v60 offset:32
	s_waitcnt vmcnt(7) lgkmcnt(1)
	v_mfma_f32_32x32x16_f16 v[0:15], v[0:3], v[16:19], 0
	ds_read_b128 v[20:23], v60 offset:8704
	ds_read_b128 v[70:73], v60 offset:8736
	s_add_i32 s0, s3, 32
	s_mov_b32 s4, 0xc350
	s_waitcnt lgkmcnt(1)
	v_mfma_f32_32x32x16_f16 v[16:31], v[20:23], v[16:19], 0
	s_waitcnt vmcnt(6)
	v_mfma_f32_32x32x16_f16 v[0:15], v[66:69], v[56:59], v[0:15]
	s_waitcnt lgkmcnt(0)
	v_mfma_f32_32x32x16_f16 v[16:31], v[70:73], v[56:59], v[16:31]
	ds_read_b128 v[56:59], v60 offset:64
	ds_read_b128 v[66:69], v60 offset:96
	s_waitcnt vmcnt(5) lgkmcnt(1)
	v_mfma_f32_32x32x16_f16 v[0:15], v[56:59], v[52:55], v[0:15]
	ds_read_b128 v[56:59], v60 offset:8768
	ds_read_b128 v[70:73], v60 offset:8800
	s_waitcnt lgkmcnt(1)
	v_mfma_f32_32x32x16_f16 v[16:31], v[56:59], v[52:55], v[16:31]
	s_waitcnt vmcnt(4)
	v_mfma_f32_32x32x16_f16 v[0:15], v[66:69], v[48:51], v[0:15]
	s_waitcnt lgkmcnt(0)
	v_mfma_f32_32x32x16_f16 v[16:31], v[70:73], v[48:51], v[16:31]
	ds_read_b128 v[48:51], v60 offset:128
	ds_read_b128 v[52:55], v60 offset:160
	s_waitcnt vmcnt(3) lgkmcnt(1)
	v_mfma_f32_32x32x16_f16 v[0:15], v[48:51], v[44:47], v[0:15]
	ds_read_b128 v[48:51], v60 offset:8832
	ds_read_b128 v[56:59], v60 offset:8864
	s_waitcnt lgkmcnt(1)
	v_mfma_f32_32x32x16_f16 v[16:31], v[48:51], v[44:47], v[16:31]
	s_waitcnt vmcnt(2)
	v_mfma_f32_32x32x16_f16 v[0:15], v[52:55], v[40:43], v[0:15]
	s_waitcnt lgkmcnt(0)
	v_mfma_f32_32x32x16_f16 v[16:31], v[56:59], v[40:43], v[16:31]
	ds_read_b128 v[40:43], v60 offset:192
	ds_read_b128 v[44:47], v60 offset:224
	s_waitcnt vmcnt(1) lgkmcnt(1)
	v_mfma_f32_32x32x16_f16 v[0:15], v[40:43], v[36:39], v[0:15]
	ds_read_b128 v[40:43], v60 offset:8896
	ds_read_b128 v[48:51], v60 offset:8928
	s_waitcnt lgkmcnt(1)
	v_mfma_f32_32x32x16_f16 v[16:31], v[40:43], v[36:39], v[16:31]
	v_lshl_or_b32 v36, v64, 5, v65
	v_lshlrev_b32_e32 v37, 2, v36
	global_load_dword v37, v37, s[14:15] nt
	s_waitcnt vmcnt(1)
	v_mfma_f32_32x32x16_f16 v[0:15], v[44:47], v[32:35], v[0:15]
	v_bfrev_b32_e32 v45, 1
	s_waitcnt lgkmcnt(0)
	v_mfma_f32_32x32x16_f16 v[16:31], v[48:51], v[32:35], v[16:31]
	s_waitcnt vmcnt(0)
	s_add_i32 s5, s3, 49
	s_cmp_le_u32 s5, s4
	s_cbranch_scc1 .Lfast_sum_l2
	s_nop 7
	v_add_f32_e32 v1, v37, v1
	s_nop 1
	v_add_f32_e32 v26, v37, v0
	v_mul_u32_u24_e32 v0, 0x440, v63
	v_lshl_add_u32 v0, v36, 1, v0
	ds_read_u16 v27, v0 offset:17408
	ds_read_u16 v28, v0 offset:17680
	ds_read_u16 v29, v0 offset:17952
	ds_read_u16 v30, v0 offset:18224
	ds_read_u16 v31, v0 offset:19584
	ds_read_u16 v32, v0 offset:19856
	ds_read_u16 v33, v0 offset:20128
	ds_read_u16 v34, v0 offset:20400
	ds_read_u16 v35, v0 offset:26112
	ds_read_u16 v38, v0 offset:26384
	ds_read_u16 v39, v0 offset:26656
	ds_read_u16 v40, v0 offset:26928
	ds_read_u16 v41, v0 offset:28288
	ds_read_u16 v42, v0 offset:28560
	ds_read_u16 v43, v0 offset:28832
	ds_read_u16 v44, v0 offset:29104
	s_waitcnt lgkmcnt(14)
	v_cvt_f32_f16_e32 v27, v27
	s_waitcnt lgkmcnt(7)
	v_cvt_f32_f16_e32 v35, v35
	v_add_f32_e32 v16, v37, v16
	v_lshlrev_b32_e32 v25, 2, v63
	v_add_f32_e32 v26, v26, v27
	v_add_f32_e32 v16, v16, v35
	v_max_f32_e32 v26, 0, v26
	v_max_f32_e32 v27, 0, v16
	v_add_u32_e32 v16, s3, v25
	v_add_f32_e32 v26, 0, v26
	v_cmp_gt_i32_e32 vcc, s4, v16
	v_add_u32_e32 v35, s0, v25
	v_add_f32_e32 v17, v37, v17
	v_cndmask_b32_e32 v26, 0, v26, vcc
	v_cmp_gt_i32_e32 vcc, s4, v35
	s_waitcnt lgkmcnt(6)
	v_cvt_f32_f16_e32 v35, v38
	v_add_f32_e32 v2, v37, v2
	v_cndmask_b32_e32 v27, v45, v27, vcc
	v_add_f32_e32 v26, v26, v27
	v_cvt_f32_f16_e32 v27, v28
	v_or_b32_e32 v28, 1, v25
	v_add_f32_e32 v17, v17, v35
	v_max_f32_e32 v17, 0, v17
	v_add_f32_e32 v1, v1, v27
	v_max_f32_e32 v1, 0, v1
	v_add_u32_e32 v27, s3, v28
	v_add_f32_e32 v1, v26, v1
	v_cmp_gt_i32_e32 vcc, s4, v27
	s_waitcnt lgkmcnt(5)
	v_cvt_f32_f16_e32 v27, v39
	v_add_f32_e32 v3, v37, v3
	v_cndmask_b32_e32 v1, v26, v1, vcc
	v_add_u32_e32 v26, s0, v28
	v_add_f32_e32 v17, v17, v1
	v_cmp_gt_i32_e32 vcc, s4, v26
	v_or_b32_e32 v26, 2, v25
	v_add_f32_e32 v4, v37, v4
	v_cndmask_b32_e32 v1, v1, v17, vcc
	v_cvt_f32_f16_e32 v17, v29
	v_add_f32_e32 v8, v37, v8
	v_add_f32_e32 v2, v2, v17
	v_max_f32_e32 v2, 0, v2
	v_add_f32_e32 v17, v37, v18
	v_add_u32_e32 v18, s3, v26
	v_add_f32_e32 v2, v1, v2
	v_cmp_gt_i32_e32 vcc, s4, v18
	v_add_f32_e32 v17, v17, v27
	s_waitcnt lgkmcnt(4)
	v_cvt_f32_f16_e32 v18, v40
	v_cndmask_b32_e32 v1, v1, v2, vcc
	v_add_u32_e32 v2, s0, v26
	v_cmp_gt_i32_e32 vcc, s4, v2
	v_cvt_f32_f16_e32 v2, v30
	v_max_f32_e32 v17, 0, v17
	v_add_f32_e32 v17, v17, v1
	v_cndmask_b32_e32 v1, v1, v17, vcc
	v_or_b32_e32 v17, 3, v25
	v_add_f32_e32 v2, v3, v2
	v_add_f32_e32 v3, v37, v19
	v_max_f32_e32 v2, 0, v2
	v_add_f32_e32 v3, v3, v18
	v_add_u32_e32 v18, s3, v17
	v_add_f32_e32 v2, v1, v2
	v_cmp_gt_i32_e32 vcc, s4, v18
	v_max_f32_e32 v3, 0, v3
	v_or_b32_e32 v19, 16, v25
	v_cndmask_b32_e32 v1, v1, v2, vcc
	v_add_u32_e32 v2, s0, v17
	v_cmp_gt_i32_e32 vcc, s4, v2
	v_cvt_f32_f16_e32 v2, v31
	s_waitcnt lgkmcnt(3)
	v_cvt_f32_f16_e32 v17, v41
	v_add_f32_e32 v3, v3, v1
	v_cndmask_b32_e32 v1, v1, v3, vcc
	v_or_b32_e32 v3, 8, v25
	v_add_f32_e32 v2, v4, v2
	v_add_f32_e32 v4, v37, v20
	v_max_f32_e32 v2, 0, v2
	v_add_f32_e32 v4, v4, v17
	v_add_u32_e32 v17, s3, v3
	v_add_f32_e32 v2, v1, v2
	v_cmp_gt_i32_e32 vcc, s4, v17
	v_max_f32_e32 v4, 0, v4
	s_nop 0
	v_cndmask_b32_e32 v1, v1, v2, vcc
	v_add_u32_e32 v2, s0, v3
	v_cmp_gt_i32_e32 vcc, s4, v2
	v_cvt_f32_f16_e32 v2, v32
	v_add_f32_e32 v3, v4, v1
	v_add_f32_e32 v4, v37, v5
	s_waitcnt lgkmcnt(2)
	v_cvt_f32_f16_e32 v5, v42
	v_cndmask_b32_e32 v1, v1, v3, vcc
	v_or_b32_e32 v3, 9, v25
	v_add_f32_e32 v2, v4, v2
	v_add_f32_e32 v4, v37, v21
	v_max_f32_e32 v2, 0, v2
	v_add_f32_e32 v4, v4, v5
	v_add_u32_e32 v5, s3, v3
	v_add_f32_e32 v2, v1, v2
	v_cmp_gt_i32_e32 vcc, s4, v5
	s_waitcnt lgkmcnt(1)
	v_cvt_f32_f16_e32 v5, v43
	v_max_f32_e32 v4, 0, v4
	v_cndmask_b32_e32 v1, v1, v2, vcc
	v_add_u32_e32 v2, s0, v3
	v_cmp_gt_i32_e32 vcc, s4, v2
	v_cvt_f32_f16_e32 v2, v33
	v_add_f32_e32 v3, v4, v1
	v_add_f32_e32 v4, v37, v6
	v_cndmask_b32_e32 v1, v1, v3, vcc
	v_or_b32_e32 v3, 10, v25
	v_add_f32_e32 v2, v4, v2
	v_add_f32_e32 v4, v37, v22
	v_max_f32_e32 v2, 0, v2
	v_add_f32_e32 v4, v4, v5
	v_add_u32_e32 v5, s3, v3
	v_add_f32_e32 v2, v1, v2
	v_cmp_gt_i32_e32 vcc, s4, v5
	s_waitcnt lgkmcnt(0)
	v_cvt_f32_f16_e32 v5, v44
	v_max_f32_e32 v4, 0, v4
	v_cndmask_b32_e32 v1, v1, v2, vcc
	v_add_u32_e32 v2, s0, v3
	v_cmp_gt_i32_e32 vcc, s4, v2
	v_cvt_f32_f16_e32 v2, v34
	v_add_f32_e32 v3, v4, v1
	v_add_f32_e32 v4, v37, v7
	v_cndmask_b32_e32 v1, v1, v3, vcc
	v_or_b32_e32 v3, 11, v25
	v_add_f32_e32 v2, v4, v2
	v_add_f32_e32 v4, v37, v23
	v_max_f32_e32 v2, 0, v2
	v_add_f32_e32 v4, v4, v5
	v_add_u32_e32 v5, s3, v3
	v_add_f32_e32 v2, v1, v2
	v_cmp_gt_i32_e32 vcc, s4, v5
	v_max_f32_e32 v4, 0, v4
	s_nop 0
	v_cndmask_b32_e32 v1, v1, v2, vcc
	v_add_u32_e32 v2, s0, v3
	v_add_f32_e32 v3, v4, v1
	v_cmp_gt_i32_e32 vcc, s4, v2
	s_nop 1
	v_cndmask_b32_e32 v1, v1, v3, vcc
	ds_read_u16 v2, v0 offset:30464
	ds_read_u16 v3, v0 offset:21760
	ds_read_u16 v4, v0 offset:22032
	ds_read_u16 v5, v0 offset:22304
	ds_read_u16 v6, v0 offset:22576
	ds_read_u16 v7, v0 offset:23936
	ds_read_u16 v17, v0 offset:24208
	ds_read_u16 v18, v0 offset:24480
	ds_read_u16 v0, v0 offset:24752
	s_waitcnt lgkmcnt(7)
	v_cvt_f32_f16_e32 v3, v3
	v_cvt_f32_f16_e32 v2, v2
	v_add_f32_e32 v3, v8, v3
	v_add_f32_e32 v8, v37, v24
	v_max_f32_e32 v3, 0, v3
	v_add_f32_e32 v2, v8, v2
	v_add_u32_e32 v8, s3, v19
	v_add_f32_e32 v3, v1, v3
	v_cmp_gt_i32_e32 vcc, s4, v8
	v_max_f32_e32 v2, 0, v2
	s_waitcnt lgkmcnt(0)
	v_cvt_f32_f16_e32 v0, v0
	v_cndmask_b32_e32 v1, v1, v3, vcc
	v_add_u32_e32 v3, s0, v19
	v_cmp_gt_i32_e64 s[0:1], s4, v3
	v_cvt_f32_f16_e32 v3, v4
	v_cmp_gt_u32_e32 vcc, 32, v62
	v_add_f32_e32 v2, v2, v1
	s_and_b64 s[0:1], vcc, s[0:1]
	v_cndmask_b32_e64 v1, v1, v2, s[0:1]
	v_add_f32_e32 v2, v37, v9
	v_add_f32_e32 v2, v2, v3
	v_cvt_f32_f16_e32 v4, v5
	v_max_f32_e32 v2, 0, v2
	v_add_u32_e32 v3, 17, v16
	v_add_f32_e32 v2, v1, v2
	v_cmp_gt_i32_e64 s[0:1], s4, v3
	v_add_u32_e32 v3, 18, v16
	s_nop 0
	v_cndmask_b32_e64 v1, v1, v2, s[0:1]
	v_add_f32_e32 v2, v37, v10
	v_add_f32_e32 v2, v2, v4
	v_cvt_f32_f16_e32 v4, v6
	v_max_f32_e32 v2, 0, v2
	v_add_f32_e32 v2, v1, v2
	v_cmp_gt_i32_e64 s[0:1], s4, v3
	v_add_u32_e32 v3, 19, v16
	s_nop 0
	v_cndmask_b32_e64 v1, v1, v2, s[0:1]
	v_add_f32_e32 v2, v37, v11
	v_add_f32_e32 v2, v2, v4
	v_cvt_f32_f16_e32 v4, v7
	v_max_f32_e32 v2, 0, v2
	v_add_f32_e32 v2, v1, v2
	v_cmp_gt_i32_e64 s[0:1], s4, v3
	v_add_u32_e32 v3, 24, v16
	s_nop 0
	v_cndmask_b32_e64 v1, v1, v2, s[0:1]
	v_add_f32_e32 v2, v37, v12
	v_add_f32_e32 v2, v2, v4
	v_cvt_f32_f16_e32 v4, v17
	v_max_f32_e32 v2, 0, v2
	v_add_f32_e32 v2, v1, v2
	v_cmp_gt_i32_e64 s[0:1], s4, v3
	v_add_u32_e32 v3, 25, v16
	s_nop 0
	v_cndmask_b32_e64 v1, v1, v2, s[0:1]
	v_add_f32_e32 v2, v37, v13
	v_add_f32_e32 v2, v2, v4
	v_cvt_f32_f16_e32 v4, v18
	v_max_f32_e32 v2, 0, v2
	v_add_f32_e32 v2, v1, v2
	v_cmp_gt_i32_e64 s[0:1], s4, v3
	v_add_u32_e32 v3, 26, v16
	s_nop 0
	v_cndmask_b32_e64 v1, v1, v2, s[0:1]
	v_add_f32_e32 v2, v37, v14
	v_add_f32_e32 v2, v2, v4
	v_max_f32_e32 v2, 0, v2
	v_add_f32_e32 v2, v1, v2
	v_cmp_gt_i32_e64 s[0:1], s4, v3
	s_nop 1
	v_cndmask_b32_e64 v1, v1, v2, s[0:1]
	v_add_f32_e32 v2, v37, v15
	v_add_f32_e32 v0, v2, v0
	v_max_f32_e32 v0, 0, v0
	v_add_u32_e32 v2, 27, v16
	v_add_f32_e32 v0, v1, v0
	v_cmp_gt_i32_e64 s[0:1], s4, v2
	v_and_b32_e32 v2, 64, v61
	v_add_u32_e32 v2, 64, v2
	v_cndmask_b32_e64 v0, v1, v0, s[0:1]

_Z7k_headsPKfS0_S0_S0_S0_Pf:
	s_load_dwordx8 s[4:11], s[0:1], 0x8
	s_load_dwordx2 s[12:13], s[0:1], 0x0
	s_load_dwordx2 s[14:15], s[0:1], 0x28
	v_lshrrev_b32_e32 v36, 2, v0
	s_movk_i32 s2, 0x100
	v_lshlrev_b32_e32 v34, 9, v36
	v_mov_b32_e32 v35, 0
	s_waitcnt lgkmcnt(0)
	v_lshl_add_u64 v[2:3], s[4:5], 0, v[34:35]
	v_mov_b32_e32 v1, s9
	v_cmp_gt_u32_e32 vcc, s2, v0
	v_and_b32_e32 v37, 3, v0
	v_lshlrev_b32_e32 v34, 7, v37
	v_cndmask_b32_e32 v3, v1, v3, vcc
	v_mov_b32_e32 v1, s8
	v_cndmask_b32_e32 v2, v1, v2, vcc
	v_lshl_add_u64 v[38:39], v[2:3], 0, v[34:35]
	global_load_dwordx4 v[18:21], v[38:39], off offset:48
	global_load_dwordx4 v[22:25], v[38:39], off offset:32
	global_load_dwordx4 v[26:29], v[38:39], off offset:16
	global_load_dwordx4 v[30:33], v[38:39], off
	global_load_dwordx4 v[2:5], v[38:39], off offset:112
	global_load_dwordx4 v[6:9], v[38:39], off offset:96
	global_load_dwordx4 v[10:13], v[38:39], off offset:80
	global_load_dwordx4 v[14:17], v[38:39], off offset:64
	v_min_u32_e32 v1, 63, v36
	v_lshlrev_b32_e32 v38, 2, v1
	v_mov_b32_e32 v39, v35
	v_lshl_add_u64 v[38:39], s[6:7], 0, v[38:39]
	v_mov_b32_e32 v1, s11
	v_cndmask_b32_e32 v39, v1, v39, vcc
	v_mov_b32_e32 v1, s10
	v_cndmask_b32_e32 v38, v1, v38, vcc
	global_load_dword v38, v[38:39], off
	s_movk_i32 s2, 0x80
	v_cmp_gt_u32_e32 vcc, s2, v0
	s_and_saveexec_b64 s[2:3], vcc
	s_cbranch_execz .LBB4_2
	v_mov_b32_e32 v1, v35
	v_lshl_add_u64 v[40:41], v[0:1], 2, s[12:13]
	global_load_dword v1, v[40:41], off
	global_load_dword v35, v[40:41], off offset:512
	global_load_dword v39, v[40:41], off offset:1024
	global_load_dword v42, v[40:41], off offset:1536
	global_load_dword v43, v[40:41], off offset:2048
	global_load_dword v44, v[40:41], off offset:2560
	global_load_dword v45, v[40:41], off offset:3072
	global_load_dword v46, v[40:41], off offset:3584
	s_movk_i32 s4, 0x1000
	v_add_co_u32_e32 v40, vcc, s4, v40
	s_waitcnt vmcnt(7)
	v_add_f32_e32 v1, 0, v1
	v_addc_co_u32_e32 v41, vcc, 0, v41, vcc
	global_load_dword v47, v[40:41], off
	global_load_dword v48, v[40:41], off offset:512
	global_load_dword v49, v[40:41], off offset:1024
	global_load_dword v50, v[40:41], off offset:1536
	global_load_dword v51, v[40:41], off offset:2048
	global_load_dword v52, v[40:41], off offset:2560
	global_load_dword v53, v[40:41], off offset:3072
	global_load_dword v54, v[40:41], off offset:3584
	s_waitcnt vmcnt(14)
	v_add_f32_e32 v1, v1, v35
	s_waitcnt vmcnt(13)
	v_add_f32_e32 v1, v1, v39
	s_waitcnt vmcnt(12)
	v_add_f32_e32 v1, v1, v42
	s_waitcnt vmcnt(11)
	v_add_f32_e32 v1, v1, v43
	s_waitcnt vmcnt(10)
	v_add_f32_e32 v1, v1, v44
	s_waitcnt vmcnt(9)
	v_add_f32_e32 v1, v1, v45
	s_waitcnt vmcnt(8)
	v_add_f32_e32 v1, v1, v46
	v_lshlrev_b32_e32 v35, 2, v0
	s_waitcnt vmcnt(7)
	v_add_f32_e32 v1, v1, v47
	s_waitcnt vmcnt(6)
	v_add_f32_e32 v1, v1, v48
	s_waitcnt vmcnt(5)
	v_add_f32_e32 v1, v1, v49
	s_waitcnt vmcnt(4)
	v_add_f32_e32 v1, v1, v50
	s_waitcnt vmcnt(3)
	v_add_f32_e32 v1, v1, v51
	s_waitcnt vmcnt(2)
	v_add_f32_e32 v1, v1, v52
	s_waitcnt vmcnt(1)
	v_add_f32_e32 v1, v1, v53
	s_waitcnt vmcnt(0)
	v_add_f32_e32 v1, v1, v54
	v_mul_f32_e32 v1, 0x37a7c5ac, v1
	ds_write_b32 v35, v1
.LBB4_2:
	s_or_b64 exec, exec, s[2:3]
	s_waitcnt lgkmcnt(0)
	s_barrier
	ds_read_b128 v[40:43], v34
	ds_read_b128 v[44:47], v34 offset:16
	ds_read_b128 v[48:51], v34 offset:32
	ds_read_b128 v[52:55], v34 offset:48
	s_movk_i32 s2, 0x104
	s_waitcnt vmcnt(5) lgkmcnt(3)
	v_mul_f32_e32 v1, v31, v41
	v_fmac_f32_e32 v1, v30, v40
	s_waitcnt lgkmcnt(2)
	v_mul_f32_e32 v27, v27, v45
	v_fmac_f32_e32 v1, v32, v42
	v_fmac_f32_e32 v27, v26, v44
	s_waitcnt lgkmcnt(1)
	v_mul_f32_e32 v23, v23, v49
	v_fmac_f32_e32 v1, v33, v43
	v_fmac_f32_e32 v27, v28, v46
	v_fmac_f32_e32 v23, v22, v48
	s_waitcnt lgkmcnt(0)
	v_mul_f32_e32 v19, v19, v53
	v_add_f32_e32 v1, 0, v1
	v_fmac_f32_e32 v27, v29, v47
	v_fmac_f32_e32 v23, v24, v50
	v_fmac_f32_e32 v19, v18, v52
	v_add_f32_e32 v1, v1, v27
	v_fmac_f32_e32 v23, v25, v51
	v_fmac_f32_e32 v19, v20, v54
	v_add_f32_e32 v1, v1, v23
	ds_read_b128 v[22:25], v34 offset:64
	v_fmac_f32_e32 v19, v21, v55
	v_add_f32_e32 v1, v1, v19
	ds_read_b128 v[18:21], v34 offset:80
	v_cmp_gt_u32_e64 s[2:3], s2, v0
	s_waitcnt vmcnt(1) lgkmcnt(1)
	v_mul_f32_e32 v15, v15, v23
	v_fmac_f32_e32 v15, v14, v22
	v_fmac_f32_e32 v15, v16, v24
	s_waitcnt lgkmcnt(0)
	v_mul_f32_e32 v11, v11, v19
	v_fmac_f32_e32 v11, v10, v18
	v_fmac_f32_e32 v15, v17, v25
	v_fmac_f32_e32 v11, v12, v20
	v_add_f32_e32 v1, v1, v15
	ds_read_b128 v[14:17], v34 offset:96
	v_fmac_f32_e32 v11, v13, v21
	v_add_f32_e32 v1, v1, v11
	ds_read_b128 v[10:13], v34 offset:112
	s_waitcnt lgkmcnt(1)
	v_mul_f32_e32 v7, v7, v15
	v_fmac_f32_e32 v7, v6, v14
	v_fmac_f32_e32 v7, v8, v16
	s_waitcnt lgkmcnt(0)
	v_mul_f32_e32 v3, v3, v11
	v_fmac_f32_e32 v3, v2, v10
	v_mbcnt_lo_u32_b32 v2, -1, 0
	v_fmac_f32_e32 v7, v9, v17
	v_fmac_f32_e32 v3, v4, v12
	v_mbcnt_hi_u32_b32 v2, -1, v2
	v_add_f32_e32 v1, v1, v7
	v_fmac_f32_e32 v3, v5, v13
	v_and_b32_e32 v4, 64, v2
	v_add_f32_e32 v1, v1, v3
	v_xor_b32_e32 v3, 1, v2
	v_add_u32_e32 v4, 64, v4
	v_cmp_lt_i32_e32 vcc, v3, v4
	s_nop 1
	v_cndmask_b32_e32 v3, v2, v3, vcc
	v_lshlrev_b32_e32 v3, 2, v3
	ds_bpermute_b32 v3, v3, v1
	s_waitcnt lgkmcnt(0)
	v_add_f32_e32 v1, v1, v3
	v_xor_b32_e32 v3, 2, v2
	v_cmp_lt_i32_e32 vcc, v3, v4
	s_nop 1
	v_cndmask_b32_e32 v2, v2, v3, vcc
	v_lshlrev_b32_e32 v2, 2, v2
	ds_bpermute_b32 v2, v2, v1
	v_cmp_eq_u32_e32 vcc, 0, v37
	s_and_b64 s[2:3], vcc, s[2:3]
	s_and_saveexec_b64 s[4:5], s[2:3]
	s_cbranch_execz .LBB4_4
	s_waitcnt lgkmcnt(0)
	v_add_f32_e32 v1, v1, v2
	v_lshlrev_b32_e32 v0, 2, v36
	s_waitcnt vmcnt(0)
	v_add_f32_e32 v1, v38, v1
	global_store_dword v0, v1, s[14:15]

	.amdhsa_kernel _Z7k_headsPKfS0_S0_S0_S0_Pf
		.amdhsa_group_segment_fixed_size 512
		.amdhsa_private_segment_fixed_size 0
		.amdhsa_kernarg_size 48
		.amdhsa_user_sgpr_count 2
		.amdhsa_user_sgpr_dispatch_ptr 0
		.amdhsa_user_sgpr_queue_ptr 0
		.amdhsa_user_sgpr_kernarg_segment_ptr 1
		.amdhsa_user_sgpr_dispatch_id 0
		.amdhsa_user_sgpr_kernarg_preload_length 0
		.amdhsa_user_sgpr_kernarg_preload_offset 0
		.amdhsa_user_sgpr_private_segment_size 0
		.amdhsa_uses_dynamic_stack 0
		.amdhsa_enable_private_segment 0
		.amdhsa_system_sgpr_workgroup_id_x 1
		.amdhsa_system_sgpr_workgroup_id_y 0
		.amdhsa_system_sgpr_workgroup_id_z 0
		.amdhsa_system_sgpr_workgroup_info 0
		.amdhsa_system_vgpr_workitem_id 0
		.amdhsa_next_free_vgpr 56
		.amdhsa_next_free_sgpr 16
		.amdhsa_accum_offset 56
		.amdhsa_reserve_vcc 1
		.amdhsa_float_round_mode_32 0
		.amdhsa_float_round_mode_16_64 0
		.amdhsa_float_denorm_mode_32 3
		.amdhsa_float_denorm_mode_16_64 3
		.amdhsa_dx10_clamp 1
		.amdhsa_ieee_mode 1
		.amdhsa_fp16_overflow 0
		.amdhsa_tg_split 0
		.amdhsa_exception_fp_ieee_invalid_op 0
		.amdhsa_exception_fp_denorm_src 0
		.amdhsa_exception_fp_ieee_div_zero 0
		.amdhsa_exception_fp_ieee_overflow 0
		.amdhsa_exception_fp_ieee_underflow 0
		.amdhsa_exception_fp_ieee_inexact 0
		.amdhsa_exception_int_div_zero 0
	.end_amdhsa_kernel

amdhsa.kernels:
  - .agpr_count:     0
    .args:
      - .actual_access:  read_only
        .address_space:  global
        .offset:         0
        .size:           8
        .value_kind:     global_buffer
      - .actual_access:  read_only
        .address_space:  global
        .offset:         8
        .size:           8
        .value_kind:     global_buffer
      - .actual_access:  write_only
        .address_space:  global
        .offset:         16
        .size:           8
        .value_kind:     global_buffer
      - .actual_access:  write_only
        .address_space:  global
        .offset:         24
        .size:           8
        .value_kind:     global_buffer
      - .actual_access:  read_only
        .address_space:  global
        .offset:         32
        .size:           8
        .value_kind:     global_buffer
      - .actual_access:  read_only
        .address_space:  global
        .offset:         40
        .size:           8
        .value_kind:     global_buffer
      - .actual_access:  read_only
        .address_space:  global
        .offset:         48
        .size:           8
        .value_kind:     global_buffer
      - .actual_access:  read_only
        .address_space:  global
        .offset:         56
        .size:           8
        .value_kind:     global_buffer
      - .actual_access:  read_only
        .address_space:  global
        .offset:         64
        .size:           8
        .value_kind:     global_buffer
      - .actual_access:  write_only
        .address_space:  global
        .offset:         72
        .size:           8
        .value_kind:     global_buffer
      - .actual_access:  write_only
        .address_space:  global
        .offset:         80
        .size:           8
        .value_kind:     global_buffer
      - .actual_access:  write_only
        .address_space:  global
        .offset:         88
        .size:           8
        .value_kind:     global_buffer
      - .actual_access:  write_only
        .address_space:  global
        .offset:         96
        .size:           8
        .value_kind:     global_buffer
      - .actual_access:  write_only
        .address_space:  global
        .offset:         104
        .size:           8
        .value_kind:     global_buffer
      - .actual_access:  write_only
        .address_space:  global
        .offset:         112
        .size:           8
        .value_kind:     global_buffer
      - .offset:         120
        .size:           4
        .value_kind:     hidden_block_count_x
      - .offset:         124
        .size:           4
        .value_kind:     hidden_block_count_y
      - .offset:         128
        .size:           4
        .value_kind:     hidden_block_count_z
      - .offset:         132
        .size:           2
        .value_kind:     hidden_group_size_x
      - .offset:         134
        .size:           2
        .value_kind:     hidden_group_size_y
      - .offset:         136
        .size:           2
        .value_kind:     hidden_group_size_z
      - .offset:         138
        .size:           2
        .value_kind:     hidden_remainder_x
      - .offset:         140
        .size:           2
        .value_kind:     hidden_remainder_y
      - .offset:         142
        .size:           2
        .value_kind:     hidden_remainder_z
      - .offset:         160
        .size:           8
        .value_kind:     hidden_global_offset_x
      - .offset:         168
        .size:           8
        .value_kind:     hidden_global_offset_y
      - .offset:         176
        .size:           8
        .value_kind:     hidden_global_offset_z
      - .offset:         184
        .size:           2
        .value_kind:     hidden_grid_dims
    .group_segment_fixed_size: 21520
    .kernarg_segment_align: 8
    .kernarg_segment_size: 376
    .language:       OpenCL C
    .language_version:
      - 2
      - 0
    .max_flat_workgroup_size: 1024
    .name:           _Z11k_chunksortPKiS0_PjS1_PKfS3_S3_S3_S3_PDF16_S4_PfS5_S4_Ph
    .private_segment_fixed_size: 0
    .sgpr_count:     32
    .sgpr_spill_count: 0
    .symbol:         _Z11k_chunksortPKiS0_PjS1_PKfS3_S3_S3_S3_PDF16_S4_PfS5_S4_Ph.kd
    .uniform_work_group_size: 1
    .uses_dynamic_stack: false
    .vgpr_count:     38
    .vgpr_spill_count: 0
    .wavefront_size: 64
  - .agpr_count:     0
    .args:
      - .actual_access:  read_only
        .address_space:  global
        .offset:         0
        .size:           8
        .value_kind:     global_buffer
      - .actual_access:  read_only
        .address_space:  global
        .offset:         8
        .size:           8
        .value_kind:     global_buffer
      - .actual_access:  read_only
        .address_space:  global
        .offset:         16
        .size:           8
        .value_kind:     global_buffer
      - .actual_access:  write_only
        .address_space:  global
        .offset:         24
        .size:           8
        .value_kind:     global_buffer
      - .actual_access:  write_only
        .address_space:  global
        .offset:         32
        .size:           8
        .value_kind:     global_buffer
      - .actual_access:  write_only
        .address_space:  global
        .offset:         40
        .size:           8
        .value_kind:     global_buffer
      - .actual_access:  write_only
        .address_space:  global
        .offset:         48
        .size:           8
        .value_kind:     global_buffer
    .group_segment_fixed_size: 22536
    .kernarg_segment_align: 8
    .kernarg_segment_size: 56
    .language:       OpenCL C
    .language_version:
      - 2
      - 0
    .max_flat_workgroup_size: 1024
    .name:           _Z5k_csrPKjS0_PKfPjPfPDF16_P15HIP_vector_typeIjLj4EE
    .private_segment_fixed_size: 0
    .sgpr_count:     44
    .sgpr_spill_count: 0
    .symbol:         _Z5k_csrPKjS0_PKfPjPfPDF16_P15HIP_vector_typeIjLj4EE.kd
    .uniform_work_group_size: 1
    .uses_dynamic_stack: false
    .vgpr_count:     48
    .vgpr_spill_count: 0
    .wavefront_size: 64
  - .agpr_count:     0
    .args:
      - .actual_access:  read_only
        .address_space:  global
        .offset:         0
        .size:           8
        .value_kind:     global_buffer
      - .actual_access:  read_only
        .address_space:  global
        .offset:         8
        .size:           8
        .value_kind:     global_buffer
      - .actual_access:  read_only
        .address_space:  global
        .offset:         16
        .size:           8
        .value_kind:     global_buffer
      - .actual_access:  read_only
        .address_space:  global
        .offset:         24
        .size:           8
        .value_kind:     global_buffer
      - .actual_access:  read_only
        .address_space:  global
        .offset:         32
        .size:           8
        .value_kind:     global_buffer
      - .actual_access:  read_only
        .address_space:  global
        .offset:         40
        .size:           8
        .value_kind:     global_buffer
      - .actual_access:  read_only
        .address_space:  global
        .offset:         48
        .size:           8
        .value_kind:     global_buffer
      - .actual_access:  write_only
        .address_space:  global
        .offset:         56
        .size:           8
        .value_kind:     global_buffer
      - .actual_access:  write_only
        .address_space:  global
        .offset:         64
        .size:           8
        .value_kind:     global_buffer
    .group_segment_fixed_size: 36112
    .kernarg_segment_align: 8
    .kernarg_segment_size: 72
    .language:       OpenCL C
    .language_version:
      - 2
      - 0
    .max_flat_workgroup_size: 256
    .name:           _Z8k_layer1PKfPKDF16_PK15HIP_vector_typeIjLj4EEPKjS0_S2_S0_PhPf
    .private_segment_fixed_size: 0
    .sgpr_count:     30
    .sgpr_spill_count: 0
    .symbol:         _Z8k_layer1PKfPKDF16_PK15HIP_vector_typeIjLj4EEPKjS0_S2_S0_PhPf.kd
    .uniform_work_group_size: 1
    .uses_dynamic_stack: false
    .vgpr_count:     128
    .vgpr_spill_count: 0
    .wavefront_size: 64
  - .agpr_count:     0
    .args:
      - .actual_access:  read_only
        .address_space:  global
        .offset:         0
        .size:           8
        .value_kind:     global_buffer
      - .actual_access:  read_only
        .address_space:  global
        .offset:         8
        .size:           8
        .value_kind:     global_buffer
      - .actual_access:  read_only
        .address_space:  global
        .offset:         16
        .size:           8
        .value_kind:     global_buffer
      - .actual_access:  read_only
        .address_space:  global
        .offset:         24
        .size:           8
        .value_kind:     global_buffer
      - .actual_access:  read_only
        .address_space:  global
        .offset:         32
        .size:           8
        .value_kind:     global_buffer
      - .actual_access:  read_only
        .address_space:  global
        .offset:         40
        .size:           8
        .value_kind:     global_buffer
      - .actual_access:  read_only
        .address_space:  global
        .offset:         48
        .size:           8
        .value_kind:     global_buffer
      - .address_space:  global
        .offset:         56
        .size:           8
        .value_kind:     global_buffer
    .group_segment_fixed_size: 39168
    .kernarg_segment_align: 8
    .kernarg_segment_size: 64
    .language:       OpenCL C
    .language_version:
      - 2
      - 0
    .max_flat_workgroup_size: 256
    .name:           _Z8k_layer2PKhPKfPK15HIP_vector_typeIjLj4EEPKjS2_PKDF16_S2_Pf
    .private_segment_fixed_size: 0
    .sgpr_count:     27
    .sgpr_spill_count: 0
    .symbol:         _Z8k_layer2PKhPKfPK15HIP_vector_typeIjLj4EEPKjS2_PKDF16_S2_Pf.kd
    .uniform_work_group_size: 1
    .uses_dynamic_stack: false
    .vgpr_count:     112
    .vgpr_spill_count: 0
    .wavefront_size: 64
  - .agpr_count:     0
    .args:
      - .actual_access:  read_only
        .address_space:  global
        .offset:         0
        .size:           8
        .value_kind:     global_buffer
      - .actual_access:  read_only
        .address_space:  global
        .offset:         8
        .size:           8
        .value_kind:     global_buffer
      - .actual_access:  read_only
        .address_space:  global
        .offset:         16
        .size:           8
        .value_kind:     global_buffer
      - .actual_access:  read_only
        .address_space:  global
        .offset:         24
        .size:           8
        .value_kind:     global_buffer
      - .actual_access:  read_only
        .address_space:  global
        .offset:         32
        .size:           8
        .value_kind:     global_buffer
      - .actual_access:  write_only
        .address_space:  global
        .offset:         40
        .size:           8
        .value_kind:     global_buffer
    .group_segment_fixed_size: 512
    .kernarg_segment_align: 8
    .kernarg_segment_size: 48
    .language:       OpenCL C
    .language_version:
      - 2
      - 0
    .max_flat_workgroup_size: 320
    .name:           _Z7k_headsPKfS0_S0_S0_S0_Pf
    .private_segment_fixed_size: 0
    .sgpr_count:     22
    .sgpr_spill_count: 0
    .symbol:         _Z7k_headsPKfS0_S0_S0_S0_Pf.kd
    .uniform_work_group_size: 1
    .uses_dynamic_stack: false
    .vgpr_count:     56
    .vgpr_spill_count: 0
    .wavefront_size: 64
